# P7: the 13 per-lane candidate look-ups (byte table, then two partial scores each) read together instead of 13 exec-masked blocks with two LDS round trips each
# speedup vs baseline: 1.0499x; 1.0074x over previous
; #define LAS __attribute__((address_space(3)))
; #define LDS_WAIT() asm volatile("s_waitcnt lgkmcnt(0)" ::: "memory")
; __device__ __forceinline__ void topk_task(const Frame& F, int l, int tb, int h, const LAS unsigned char* kl, LAS float* tl, const LAS unsigned char* cab) {
;     ...
;     LDS_WAIT(); asm volatile("" ::: "memory");
;     const LAS float* t0l = tl + (0 * 16 + c) * TL_STRIDE; const LAS float* t1l = tl + (16 + c) * TL_STRIDE;
;     float res[16];
; #pragma unroll
;     for (int j = 0; j < 16; ++j) {
;         const int cid = j * 4 + rq; const unsigned ab = cab[cid < 50 ? cid : 0];
;         const float sum = t0l[ab >> 4] + t1l[ab & 15];
;         res[j] = (j < 13 && cid < 50) ? embed_idx<63u>(sum, (unsigned)cid) : NEG;
;     }
.LBB0_1013:
	s_or_b64 exec, exec, s[0:1]
	s_waitcnt lgkmcnt(0)
	v_mov_b32_e32 v0, s73
	v_mad_u32_u24 v1, v88, s7, v0
	v_add_u32_e32 v226, 0x15400, v80
	ds_read_u8 v194, v226
	ds_read_u8 v195, v226 offset:4
	ds_read_u8 v196, v226 offset:8
	ds_read_u8 v197, v226 offset:12
	ds_read_u8 v198, v226 offset:16
	ds_read_u8 v199, v226 offset:20
	ds_read_u8 v200, v226 offset:24
	ds_read_u8 v201, v226 offset:28
	ds_read_u8 v202, v226 offset:32
	ds_read_u8 v203, v226 offset:36
	ds_read_u8 v204, v226 offset:40
	ds_read_u8 v205, v226 offset:44
	ds_read_u8 v206, v226 offset:48
	s_waitcnt lgkmcnt(0)
	v_lshrrev_b32_e32 v227, 2, v194
	v_and_b32_e32 v227, 60, v227
	v_add_u32_e32 v227, v1, v227
	v_and_b32_e32 v194, 15, v194
	v_lshl_add_u32 v194, v194, 2, v1
	v_lshrrev_b32_e32 v228, 2, v195
	v_and_b32_e32 v228, 60, v228
	v_add_u32_e32 v228, v1, v228
	v_and_b32_e32 v195, 15, v195
	v_lshl_add_u32 v195, v195, 2, v1
	v_lshrrev_b32_e32 v229, 2, v196
	v_and_b32_e32 v229, 60, v229
	v_add_u32_e32 v229, v1, v229
	v_and_b32_e32 v196, 15, v196
	v_lshl_add_u32 v196, v196, 2, v1
	v_lshrrev_b32_e32 v230, 2, v197
	v_and_b32_e32 v230, 60, v230
	v_add_u32_e32 v230, v1, v230
	v_and_b32_e32 v197, 15, v197
	v_lshl_add_u32 v197, v197, 2, v1
	v_lshrrev_b32_e32 v231, 2, v198
	v_and_b32_e32 v231, 60, v231
	v_add_u32_e32 v231, v1, v231
	v_and_b32_e32 v198, 15, v198
	v_lshl_add_u32 v198, v198, 2, v1
	v_lshrrev_b32_e32 v232, 2, v199
	v_and_b32_e32 v232, 60, v232
	v_add_u32_e32 v232, v1, v232
	v_and_b32_e32 v199, 15, v199
	v_lshl_add_u32 v199, v199, 2, v1
	v_lshrrev_b32_e32 v233, 2, v200
	v_and_b32_e32 v233, 60, v233
	v_add_u32_e32 v233, v1, v233
	v_and_b32_e32 v200, 15, v200
	v_lshl_add_u32 v200, v200, 2, v1
	v_lshrrev_b32_e32 v234, 2, v201
	v_and_b32_e32 v234, 60, v234
	v_add_u32_e32 v234, v1, v234
	v_and_b32_e32 v201, 15, v201
	v_lshl_add_u32 v201, v201, 2, v1
	v_lshrrev_b32_e32 v235, 2, v202
	v_and_b32_e32 v235, 60, v235
	v_add_u32_e32 v235, v1, v235
	v_and_b32_e32 v202, 15, v202
	v_lshl_add_u32 v202, v202, 2, v1
	v_lshrrev_b32_e32 v236, 2, v203
	v_and_b32_e32 v236, 60, v236
	v_add_u32_e32 v236, v1, v236
	v_and_b32_e32 v203, 15, v203
	v_lshl_add_u32 v203, v203, 2, v1
	v_lshrrev_b32_e32 v237, 2, v204
	v_and_b32_e32 v237, 60, v237
	v_add_u32_e32 v237, v1, v237
	v_and_b32_e32 v204, 15, v204
	v_lshl_add_u32 v204, v204, 2, v1
	v_lshrrev_b32_e32 v238, 2, v205
	v_and_b32_e32 v238, 60, v238
	v_add_u32_e32 v238, v1, v238
	v_and_b32_e32 v205, 15, v205
	v_lshl_add_u32 v205, v205, 2, v1
	v_lshrrev_b32_e32 v239, 2, v206
	v_and_b32_e32 v239, 60, v239
	v_add_u32_e32 v239, v1, v239
	v_and_b32_e32 v206, 15, v206
	v_lshl_add_u32 v206, v206, 2, v1
	ds_read_b32 v227, v227
	ds_read_b32 v194, v194 offset:1088
	ds_read_b32 v228, v228
	ds_read_b32 v195, v195 offset:1088
	ds_read_b32 v229, v229
	ds_read_b32 v196, v196 offset:1088
	ds_read_b32 v230, v230
	ds_read_b32 v197, v197 offset:1088
	ds_read_b32 v231, v231
	ds_read_b32 v198, v198 offset:1088
	ds_read_b32 v232, v232
	ds_read_b32 v199, v199 offset:1088
	ds_read_b32 v233, v233
	ds_read_b32 v200, v200 offset:1088
	ds_read_b32 v234, v234
	ds_read_b32 v201, v201 offset:1088
	ds_read_b32 v235, v235
	ds_read_b32 v202, v202 offset:1088
	ds_read_b32 v236, v236
	ds_read_b32 v203, v203 offset:1088
	ds_read_b32 v237, v237
	ds_read_b32 v204, v204 offset:1088
	ds_read_b32 v238, v238
	ds_read_b32 v205, v205 offset:1088
	ds_read_b32 v239, v239
	ds_read_b32 v206, v206 offset:1088
	s_waitcnt lgkmcnt(15)
	v_add_f32_e32 v227, v227, v194
	v_sub_u32_e32 v194, 63, v80
	v_add_u32_e32 v226, 0, v80
	v_cmp_gt_i32_e32 vcc, 0, v227
	s_nop 1
	v_cndmask_b32_e32 v194, v194, v226, vcc
	v_and_or_b32 v0, v227, s74, v194
	s_waitcnt lgkmcnt(15)
	v_add_f32_e32 v228, v228, v195
	v_sub_u32_e32 v195, 59, v80
	v_add_u32_e32 v226, 4, v80
	v_cmp_gt_i32_e32 vcc, 0, v228
	s_nop 1
	v_cndmask_b32_e32 v195, v195, v226, vcc
	v_and_or_b32 v2, v228, s74, v195
	s_waitcnt lgkmcnt(15)
	v_add_f32_e32 v229, v229, v196
	v_sub_u32_e32 v196, 55, v80
	v_add_u32_e32 v226, 8, v80
	v_cmp_gt_i32_e32 vcc, 0, v229
	s_nop 1
	v_cndmask_b32_e32 v196, v196, v226, vcc
	v_and_or_b32 v3, v229, s74, v196
	s_waitcnt lgkmcnt(15)
	v_add_f32_e32 v230, v230, v197
	v_sub_u32_e32 v197, 51, v80
	v_add_u32_e32 v226, 12, v80
	v_cmp_gt_i32_e32 vcc, 0, v230
	s_nop 1
	v_cndmask_b32_e32 v197, v197, v226, vcc
	v_and_or_b32 v4, v230, s74, v197
	s_waitcnt lgkmcnt(15)
	v_add_f32_e32 v231, v231, v198
	v_sub_u32_e32 v198, 47, v80
	v_add_u32_e32 v226, 16, v80
	v_cmp_gt_i32_e32 vcc, 0, v231
	s_nop 1
	v_cndmask_b32_e32 v198, v198, v226, vcc
	v_and_or_b32 v5, v231, s74, v198
	s_waitcnt lgkmcnt(14)
	v_add_f32_e32 v232, v232, v199
	v_sub_u32_e32 v199, 43, v80
	v_add_u32_e32 v226, 20, v80
	v_cmp_gt_i32_e32 vcc, 0, v232
	s_nop 1
	v_cndmask_b32_e32 v199, v199, v226, vcc
	v_and_or_b32 v6, v232, s74, v199
	s_waitcnt lgkmcnt(12)
	v_add_f32_e32 v233, v233, v200
	v_sub_u32_e32 v200, 39, v80
	v_add_u32_e32 v226, 24, v80
	v_cmp_gt_i32_e32 vcc, 0, v233
	s_nop 1
	v_cndmask_b32_e32 v200, v200, v226, vcc
	v_and_or_b32 v7, v233, s74, v200
	s_waitcnt lgkmcnt(10)
	v_add_f32_e32 v234, v234, v201
	v_sub_u32_e32 v201, 35, v80
	v_add_u32_e32 v226, 28, v80
	v_cmp_gt_i32_e32 vcc, 0, v234
	s_nop 1
	v_cndmask_b32_e32 v201, v201, v226, vcc
	v_and_or_b32 v8, v234, s74, v201
	s_waitcnt lgkmcnt(8)
	v_add_f32_e32 v235, v235, v202
	v_sub_u32_e32 v202, 31, v80
	v_add_u32_e32 v226, 32, v80
	v_cmp_gt_i32_e32 vcc, 0, v235
	s_nop 1
	v_cndmask_b32_e32 v202, v202, v226, vcc
	v_and_or_b32 v9, v235, s74, v202
	s_waitcnt lgkmcnt(6)
	v_add_f32_e32 v236, v236, v203
	v_sub_u32_e32 v203, 27, v80
	v_add_u32_e32 v226, 36, v80
	v_cmp_gt_i32_e32 vcc, 0, v236
	s_nop 1
	v_cndmask_b32_e32 v203, v203, v226, vcc
	v_and_or_b32 v10, v236, s74, v203
	s_waitcnt lgkmcnt(4)
	v_add_f32_e32 v237, v237, v204
	v_sub_u32_e32 v204, 23, v80
	v_add_u32_e32 v226, 40, v80
	v_cmp_gt_i32_e32 vcc, 0, v237
	s_nop 1
	v_cndmask_b32_e32 v204, v204, v226, vcc
	v_and_or_b32 v11, v237, s74, v204
	s_waitcnt lgkmcnt(2)
	v_add_f32_e32 v238, v238, v205
	v_sub_u32_e32 v205, 19, v80
	v_add_u32_e32 v226, 44, v80
	v_cmp_gt_i32_e32 vcc, 0, v238
	s_nop 1
	v_cndmask_b32_e32 v205, v205, v226, vcc
	v_and_or_b32 v12, v238, s74, v205
	s_waitcnt lgkmcnt(0)
	v_add_f32_e32 v239, v239, v206
	v_sub_u32_e32 v206, 15, v80
	v_add_u32_e32 v226, 48, v80
	v_cmp_gt_i32_e32 vcc, 0, v239
	s_nop 1
	v_cndmask_b32_e32 v206, v206, v226, vcc
	v_and_or_b32 v13, v239, s74, v206
	v_max_f32_e32 v13, v13, v13
	v_max_f32_e32 v13, 0xff800000, v13
	v_cmp_gt_i32_e32 vcc, 2, v80
	v_mov_b32_e32 v226, 0xff800000
	s_nop 0
	v_cndmask_b32_e32 v13, v226, v13, vcc
